# rwkv_pre S1 (Gram tiles) rewritten: wave-uniform variants, zero tiles skip MFMA/mask math, LDS reads software-pipelined
# speedup vs baseline: 1.0171x; 1.0127x over previous
.LBB0_612:
	s_or_b64 exec, exec, s[0:1]
	v_mov_b32_e32 v0, v187
	s_waitcnt lgkmcnt(0)
	s_barrier
	v_lshrrev_b32_e32 v18, 6, v0
	v_and_b32_e32 v166, 15, v0
	v_and_b32_e32 v167, 48, v0
	v_readfirstlane_b32 s2, v18
	v_mul_u32_u24_e32 v169, 0x90, v166
	v_lshrrev_b32_e32 v168, 2, v167
	s_and_b32 s3, s2, 1
	s_lshr_b32 s4, s2, 1
	v_sub_u32_e32 v172, v166, v168
	v_lshrrev_b32_e32 v168, 1, v167
	v_add_u32_e32 v173, v169, v168
	v_add_u32_e32 v169, v169, v167
	s_and_b32 s5, s4, 1
	s_mul_i32 s5, s5, 0x2400
	s_addk_i32 s5, 0x2400
	s_lshr_b32 s12, s4, 1
	s_mul_i32 s13, s12, 0x6c00
	v_add_u32_e32 v170, s5, v169
	v_add_u32_e32 v171, s13, v169
	v_add_u32_e32 v172, s12, v172
	s_cmp_eq_u32 s4, 0
	s_cbranch_scc1 .Ls1_m0
	s_mul_i32 s13, s4, 0x2400
	s_add_i32 s13, s13, 0xd800
	v_add_u32_e32 v173, s13, v173
	s_cmp_eq_u32 s3, 0
	s_cbranch_scc1 .Ls1_mx_w0
	ds_read_b128 v[2:5], v170 offset:4608
	ds_read_b128 v[6:9], v171 offset:4608
	ds_read_b128 v[10:13], v170 offset:4672
	ds_read_b128 v[14:17], v171 offset:4672
	ds_read_b128 v[174:177], v170 offset:4608
	ds_read_b128 v[178:181], v171 offset:6912
	ds_read_b128 v[240:243], v170 offset:4672
	ds_read_b128 v[244:247], v171 offset:6976
	ds_write_b64 v173, v[34:35] offset:64
	ds_write_b64 v173, v[34:35] offset:2368
	v_cmp_gt_i32_e64 s[16:17], v172, 0
	v_cmp_gt_i32_e64 s[18:19], v172, 1
	v_cmp_gt_i32_e64 s[20:21], v172, 2
	v_cmp_gt_i32_e64 s[22:23], v172, 3
	s_waitcnt lgkmcnt(8)
	v_mfma_f32_16x16x32_bf16 v[24:27], v[2:5], v[6:9], 0
	ds_read_b128 v[2:5], v170 offset:6912
	ds_read_b128 v[6:9], v171 offset:6912
	s_waitcnt lgkmcnt(8)
	v_mfma_f32_16x16x32_bf16 v[24:27], v[10:13], v[14:17], v[24:27]
	ds_read_b128 v[10:13], v170 offset:6976
	ds_read_b128 v[14:17], v171 offset:6976
	s_nop 5
	v_cndmask_b32_e64 v24, 0, v24, s[16:17]
	v_cndmask_b32_e64 v25, 0, v25, s[18:19]
	v_cndmask_b32_e64 v26, 0, v26, s[20:21]
	v_cndmask_b32_e64 v27, 0, v27, s[22:23]
	v_cvt_pk_bf16_f32 v32, v24, v25
	v_cvt_pk_bf16_f32 v33, v26, v27
	ds_write_b64 v173, v[32:33] offset:4672
	s_waitcnt lgkmcnt(9)
	v_mfma_f32_16x16x32_bf16 v[28:31], v[174:177], v[178:181], 0
	s_waitcnt lgkmcnt(7)
	v_mfma_f32_16x16x32_bf16 v[28:31], v[240:243], v[244:247], v[28:31]
	s_nop 7
	v_cvt_pk_bf16_f32 v22, v28, v29
	v_cvt_pk_bf16_f32 v23, v30, v31
	ds_write_b64 v173, v[22:23] offset:6976
	ds_write_b64 v173, v[34:35] offset:96
	ds_write_b64 v173, v[34:35] offset:2400
	ds_write_b64 v173, v[34:35] offset:4704
	v_cmp_gt_i32_e64 s[16:17], v172, 0
	v_cmp_gt_i32_e64 s[18:19], v172, 1
	v_cmp_gt_i32_e64 s[20:21], v172, 2
	v_cmp_gt_i32_e64 s[22:23], v172, 3
	s_waitcnt lgkmcnt(7)
	v_mfma_f32_16x16x32_bf16 v[24:27], v[2:5], v[6:9], 0
	s_waitcnt lgkmcnt(5)
	v_mfma_f32_16x16x32_bf16 v[24:27], v[10:13], v[14:17], v[24:27]
	s_nop 7
	v_cndmask_b32_e64 v24, 0, v24, s[16:17]
	v_cndmask_b32_e64 v25, 0, v25, s[18:19]
	v_cndmask_b32_e64 v26, 0, v26, s[20:21]
	v_cndmask_b32_e64 v27, 0, v27, s[22:23]
	v_cvt_pk_bf16_f32 v32, v24, v25
	v_cvt_pk_bf16_f32 v33, v26, v27
	ds_write_b64 v173, v[32:33] offset:7008
	s_branch .LBB0_622
.Ls1_mx_w0:
	ds_read_b128 v[2:5], v170 offset:0
	ds_read_b128 v[6:9], v171 offset:0
	ds_read_b128 v[10:13], v170 offset:64
	ds_read_b128 v[14:17], v171 offset:64
	ds_read_b128 v[174:177], v170 offset:0
	ds_read_b128 v[178:181], v171 offset:2304
	ds_read_b128 v[240:243], v170 offset:64
	ds_read_b128 v[244:247], v171 offset:2368
	v_cmp_gt_i32_e64 s[16:17], v172, 0
	v_cmp_gt_i32_e64 s[18:19], v172, 1
	v_cmp_gt_i32_e64 s[20:21], v172, 2
	v_cmp_gt_i32_e64 s[22:23], v172, 3
	s_waitcnt lgkmcnt(6)
	v_mfma_f32_16x16x32_bf16 v[24:27], v[2:5], v[6:9], 0
	ds_read_b128 v[2:5], v170 offset:0
	ds_read_b128 v[6:9], v171 offset:4608
	s_waitcnt lgkmcnt(6)
	v_mfma_f32_16x16x32_bf16 v[24:27], v[10:13], v[14:17], v[24:27]
	ds_read_b128 v[10:13], v170 offset:64
	ds_read_b128 v[14:17], v171 offset:4672
	s_nop 5
	v_cndmask_b32_e64 v24, 0, v24, s[16:17]
	v_cndmask_b32_e64 v25, 0, v25, s[18:19]
	v_cndmask_b32_e64 v26, 0, v26, s[20:21]
	v_cndmask_b32_e64 v27, 0, v27, s[22:23]
	v_cvt_pk_bf16_f32 v32, v24, v25
	v_cvt_pk_bf16_f32 v33, v26, v27
	ds_write_b64 v173, v[32:33] offset:0
	s_waitcnt lgkmcnt(7)
	v_mfma_f32_16x16x32_bf16 v[28:31], v[174:177], v[178:181], 0
	ds_read_b128 v[174:177], v170 offset:0
	ds_read_b128 v[178:181], v171 offset:6912
	s_waitcnt lgkmcnt(7)
	v_mfma_f32_16x16x32_bf16 v[28:31], v[240:243], v[244:247], v[28:31]
	ds_read_b128 v[240:243], v170 offset:64
	ds_read_b128 v[244:247], v171 offset:6976
	s_nop 5
	v_cvt_pk_bf16_f32 v22, v28, v29
	v_cvt_pk_bf16_f32 v23, v30, v31
	ds_write_b64 v173, v[22:23] offset:2304
	s_waitcnt lgkmcnt(8)
	v_mfma_f32_16x16x32_bf16 v[24:27], v[2:5], v[6:9], 0
	ds_read_b128 v[2:5], v170 offset:2304
	ds_read_b128 v[6:9], v171 offset:2304
	s_waitcnt lgkmcnt(8)
	v_mfma_f32_16x16x32_bf16 v[24:27], v[10:13], v[14:17], v[24:27]
	ds_read_b128 v[10:13], v170 offset:2368
	ds_read_b128 v[14:17], v171 offset:2368
	s_nop 5
	v_cvt_pk_bf16_f32 v32, v24, v25
	v_cvt_pk_bf16_f32 v33, v26, v27
	ds_write_b64 v173, v[32:33] offset:4608
	s_waitcnt lgkmcnt(8)
	v_mfma_f32_16x16x32_bf16 v[28:31], v[174:177], v[178:181], 0
	ds_read_b128 v[174:177], v170 offset:2304
	ds_read_b128 v[178:181], v171 offset:4608
	s_waitcnt lgkmcnt(8)
	v_mfma_f32_16x16x32_bf16 v[28:31], v[240:243], v[244:247], v[28:31]
	ds_read_b128 v[240:243], v170 offset:2368
	ds_read_b128 v[244:247], v171 offset:4672
	s_nop 5
	v_cvt_pk_bf16_f32 v22, v28, v29
	v_cvt_pk_bf16_f32 v23, v30, v31
	ds_write_b64 v173, v[22:23] offset:6912
	ds_write_b64 v173, v[34:35] offset:32
	v_cmp_gt_i32_e64 s[16:17], v172, 0
	v_cmp_gt_i32_e64 s[18:19], v172, 1
	v_cmp_gt_i32_e64 s[20:21], v172, 2
	v_cmp_gt_i32_e64 s[22:23], v172, 3
	s_waitcnt lgkmcnt(9)
	v_mfma_f32_16x16x32_bf16 v[24:27], v[2:5], v[6:9], 0
	ds_read_b128 v[2:5], v170 offset:2304
	ds_read_b128 v[6:9], v171 offset:6912
	s_waitcnt lgkmcnt(9)
	v_mfma_f32_16x16x32_bf16 v[24:27], v[10:13], v[14:17], v[24:27]
	ds_read_b128 v[10:13], v170 offset:2368
	ds_read_b128 v[14:17], v171 offset:6976
	s_nop 5
	v_cndmask_b32_e64 v24, 0, v24, s[16:17]
	v_cndmask_b32_e64 v25, 0, v25, s[18:19]
	v_cndmask_b32_e64 v26, 0, v26, s[20:21]
	v_cndmask_b32_e64 v27, 0, v27, s[22:23]
	v_cvt_pk_bf16_f32 v32, v24, v25
	v_cvt_pk_bf16_f32 v33, v26, v27
	ds_write_b64 v173, v[32:33] offset:2336
	s_waitcnt lgkmcnt(9)
	v_mfma_f32_16x16x32_bf16 v[28:31], v[174:177], v[178:181], 0
	s_waitcnt lgkmcnt(7)
	v_mfma_f32_16x16x32_bf16 v[28:31], v[240:243], v[244:247], v[28:31]
	s_nop 7
	v_cvt_pk_bf16_f32 v22, v28, v29
	v_cvt_pk_bf16_f32 v23, v30, v31
	ds_write_b64 v173, v[22:23] offset:4640
	s_waitcnt lgkmcnt(4)
	v_mfma_f32_16x16x32_bf16 v[24:27], v[2:5], v[6:9], 0
	s_waitcnt lgkmcnt(2)
	v_mfma_f32_16x16x32_bf16 v[24:27], v[10:13], v[14:17], v[24:27]
	s_nop 7
	v_cvt_pk_bf16_f32 v32, v24, v25
	v_cvt_pk_bf16_f32 v33, v26, v27
	ds_write_b64 v173, v[32:33] offset:6944
	s_branch .LBB0_622
.Ls1_m0:
	v_add_u32_e32 v173, 0x1b000, v173
	v_lshlrev_b32_e32 v182, 6, v167
	v_lshl_add_u32 v182, v166, 2, v182
	v_add_u32_e32 v182, 0x1d400, v182
	s_cmp_eq_u32 s3, 0
	s_cbranch_scc1 .Ls1_m0_w0
	ds_read_b128 v[2:5], v170 offset:4608
	ds_read_b128 v[6:9], v171 offset:4608
	ds_read_b128 v[10:13], v170 offset:4672
	ds_read_b128 v[14:17], v171 offset:4672
	ds_read_b128 v[174:177], v170 offset:4608
	ds_read_b128 v[178:181], v171 offset:6912
	ds_read_b128 v[240:243], v170 offset:4672
	ds_read_b128 v[244:247], v171 offset:6976
	ds_write_b32 v182, v1 offset:8192
	ds_write_b32 v182, v1 offset:8448
	ds_write_b32 v182, v1 offset:8704
	ds_write_b32 v182, v1 offset:8960
	ds_write_b64 v173, v[34:35] offset:64
	ds_write_b32 v182, v1 offset:8256
	ds_write_b32 v182, v1 offset:8512
	ds_write_b32 v182, v1 offset:8768
	ds_write_b32 v182, v1 offset:9024
	ds_write_b64 v173, v[34:35] offset:2368
	v_cmp_gt_i32_e64 s[16:17], v172, 0
	v_cmp_gt_i32_e64 s[18:19], v172, 1
	v_cmp_gt_i32_e64 s[20:21], v172, 2
	v_cmp_gt_i32_e64 s[22:23], v172, 3
	s_waitcnt lgkmcnt(15)
	v_mfma_f32_16x16x32_bf16 v[24:27], v[2:5], v[6:9], 0
	ds_read_b128 v[2:5], v170 offset:6912
	ds_read_b128 v[6:9], v171 offset:6912
	s_waitcnt lgkmcnt(15)
	v_mfma_f32_16x16x32_bf16 v[24:27], v[10:13], v[14:17], v[24:27]
	ds_read_b128 v[10:13], v170 offset:6976
	ds_read_b128 v[14:17], v171 offset:6976
	s_nop 5
	v_cndmask_b32_e64 v24, 0, v24, s[16:17]
	v_cndmask_b32_e64 v25, 0, v25, s[18:19]
	v_cndmask_b32_e64 v26, 0, v26, s[20:21]
	v_cndmask_b32_e64 v27, 0, v27, s[22:23]
	ds_write_b32 v182, v24 offset:8320
	ds_write_b32 v182, v25 offset:8576
	ds_write_b32 v182, v26 offset:8832
	ds_write_b32 v182, v27 offset:9088
	ds_write_b64 v173, v[34:35] offset:4672
	s_waitcnt lgkmcnt(15)
	v_mfma_f32_16x16x32_bf16 v[28:31], v[174:177], v[178:181], 0
	v_mfma_f32_16x16x32_bf16 v[28:31], v[240:243], v[244:247], v[28:31]
	s_nop 7
	ds_write_b32 v182, v28 offset:8384
	ds_write_b32 v182, v29 offset:8640
	ds_write_b32 v182, v30 offset:8896
	ds_write_b32 v182, v31 offset:9152
	v_cvt_pk_bf16_f32 v22, v28, v29
	v_cvt_pk_bf16_f32 v23, v30, v31
	ds_write_b64 v173, v[22:23] offset:6976
	ds_write_b32 v182, v1 offset:12288
	ds_write_b32 v182, v1 offset:12544
	ds_write_b32 v182, v1 offset:12800
	ds_write_b32 v182, v1 offset:13056
	ds_write_b64 v173, v[34:35] offset:96
	ds_write_b32 v182, v1 offset:12352
	ds_write_b32 v182, v1 offset:12608
	ds_write_b32 v182, v1 offset:12864
	ds_write_b32 v182, v1 offset:13120
	ds_write_b64 v173, v[34:35] offset:2400
	ds_write_b32 v182, v1 offset:12416
	ds_write_b32 v182, v1 offset:12672
	ds_write_b32 v182, v1 offset:12928
	ds_write_b32 v182, v1 offset:13184
	ds_write_b64 v173, v[34:35] offset:4704
	v_cmp_gt_i32_e64 s[16:17], v172, 0
	v_cmp_gt_i32_e64 s[18:19], v172, 1
	v_cmp_gt_i32_e64 s[20:21], v172, 2
	v_cmp_gt_i32_e64 s[22:23], v172, 3
	s_waitcnt lgkmcnt(15)
	v_mfma_f32_16x16x32_bf16 v[24:27], v[2:5], v[6:9], 0
	v_mfma_f32_16x16x32_bf16 v[24:27], v[10:13], v[14:17], v[24:27]
	s_nop 7
	v_cndmask_b32_e64 v24, 0, v24, s[16:17]
	v_cndmask_b32_e64 v25, 0, v25, s[18:19]
	v_cndmask_b32_e64 v26, 0, v26, s[20:21]
	v_cndmask_b32_e64 v27, 0, v27, s[22:23]
	ds_write_b32 v182, v24 offset:12480
	ds_write_b32 v182, v25 offset:12736
	ds_write_b32 v182, v26 offset:12992
	ds_write_b32 v182, v27 offset:13248
	ds_write_b64 v173, v[34:35] offset:7008
	s_branch .LBB0_622
.Ls1_m0_w0:
	ds_read_b128 v[2:5], v170 offset:0
	ds_read_b128 v[6:9], v171 offset:0
	ds_read_b128 v[10:13], v170 offset:64
	ds_read_b128 v[14:17], v171 offset:64
	ds_read_b128 v[174:177], v170 offset:0
	ds_read_b128 v[178:181], v171 offset:2304
	ds_read_b128 v[240:243], v170 offset:64
	ds_read_b128 v[244:247], v171 offset:2368
	v_cmp_gt_i32_e64 s[16:17], v172, 0
	v_cmp_gt_i32_e64 s[18:19], v172, 1
	v_cmp_gt_i32_e64 s[20:21], v172, 2
	v_cmp_gt_i32_e64 s[22:23], v172, 3
	s_waitcnt lgkmcnt(6)
	v_mfma_f32_16x16x32_bf16 v[24:27], v[2:5], v[6:9], 0
	ds_read_b128 v[2:5], v170 offset:0
	ds_read_b128 v[6:9], v171 offset:4608
	s_waitcnt lgkmcnt(6)
	v_mfma_f32_16x16x32_bf16 v[24:27], v[10:13], v[14:17], v[24:27]
	ds_read_b128 v[10:13], v170 offset:64
	ds_read_b128 v[14:17], v171 offset:4672
	s_nop 5
	v_cndmask_b32_e64 v24, 0, v24, s[16:17]
	v_cndmask_b32_e64 v25, 0, v25, s[18:19]
	v_cndmask_b32_e64 v26, 0, v26, s[20:21]
	v_cndmask_b32_e64 v27, 0, v27, s[22:23]
	ds_write_b32 v182, v24 offset:0
	ds_write_b32 v182, v25 offset:256
	ds_write_b32 v182, v26 offset:512
	ds_write_b32 v182, v27 offset:768
	ds_write_b64 v173, v[34:35] offset:0
	s_waitcnt lgkmcnt(11)
	v_mfma_f32_16x16x32_bf16 v[28:31], v[174:177], v[178:181], 0
	ds_read_b128 v[174:177], v170 offset:0
	ds_read_b128 v[178:181], v171 offset:6912
	s_waitcnt lgkmcnt(11)
	v_mfma_f32_16x16x32_bf16 v[28:31], v[240:243], v[244:247], v[28:31]
	ds_read_b128 v[240:243], v170 offset:64
	ds_read_b128 v[244:247], v171 offset:6976
	s_nop 5
	ds_write_b32 v182, v28 offset:64
	ds_write_b32 v182, v29 offset:320
	ds_write_b32 v182, v30 offset:576
	ds_write_b32 v182, v31 offset:832
	v_cvt_pk_bf16_f32 v22, v28, v29
	v_cvt_pk_bf16_f32 v23, v30, v31
	ds_write_b64 v173, v[22:23] offset:2304
	s_waitcnt lgkmcnt(15)
	v_mfma_f32_16x16x32_bf16 v[24:27], v[2:5], v[6:9], 0
	ds_read_b128 v[2:5], v170 offset:2304
	ds_read_b128 v[6:9], v171 offset:2304
	s_waitcnt lgkmcnt(15)
	v_mfma_f32_16x16x32_bf16 v[24:27], v[10:13], v[14:17], v[24:27]
	ds_read_b128 v[10:13], v170 offset:2368
	ds_read_b128 v[14:17], v171 offset:2368
	s_nop 5
	ds_write_b32 v182, v24 offset:128
	ds_write_b32 v182, v25 offset:384
	ds_write_b32 v182, v26 offset:640
	ds_write_b32 v182, v27 offset:896
	v_cvt_pk_bf16_f32 v32, v24, v25
	v_cvt_pk_bf16_f32 v33, v26, v27
	ds_write_b64 v173, v[32:33] offset:4608
	s_waitcnt lgkmcnt(15)
	v_mfma_f32_16x16x32_bf16 v[28:31], v[174:177], v[178:181], 0
	ds_read_b128 v[174:177], v170 offset:2304
	ds_read_b128 v[178:181], v171 offset:4608
	s_waitcnt lgkmcnt(15)
	v_mfma_f32_16x16x32_bf16 v[28:31], v[240:243], v[244:247], v[28:31]
	ds_read_b128 v[240:243], v170 offset:2368
	ds_read_b128 v[244:247], v171 offset:4672
	s_nop 5
	ds_write_b32 v182, v28 offset:192
	ds_write_b32 v182, v29 offset:448
	ds_write_b32 v182, v30 offset:704
	ds_write_b32 v182, v31 offset:960
	v_cvt_pk_bf16_f32 v22, v28, v29
	v_cvt_pk_bf16_f32 v23, v30, v31
	ds_write_b64 v173, v[22:23] offset:6912
	ds_write_b32 v182, v1 offset:4096
	ds_write_b32 v182, v1 offset:4352
	ds_write_b32 v182, v1 offset:4608
	ds_write_b32 v182, v1 offset:4864
	ds_write_b64 v173, v[34:35] offset:32
	v_cmp_gt_i32_e64 s[16:17], v172, 0
	v_cmp_gt_i32_e64 s[18:19], v172, 1
	v_cmp_gt_i32_e64 s[20:21], v172, 2
	v_cmp_gt_i32_e64 s[22:23], v172, 3
	s_waitcnt lgkmcnt(15)
	v_mfma_f32_16x16x32_bf16 v[24:27], v[2:5], v[6:9], 0
	ds_read_b128 v[2:5], v170 offset:2304
	ds_read_b128 v[6:9], v171 offset:6912
	v_mfma_f32_16x16x32_bf16 v[24:27], v[10:13], v[14:17], v[24:27]
	ds_read_b128 v[10:13], v170 offset:2368
	ds_read_b128 v[14:17], v171 offset:6976
	s_nop 5
	v_cndmask_b32_e64 v24, 0, v24, s[16:17]
	v_cndmask_b32_e64 v25, 0, v25, s[18:19]
	v_cndmask_b32_e64 v26, 0, v26, s[20:21]
	v_cndmask_b32_e64 v27, 0, v27, s[22:23]
	ds_write_b32 v182, v24 offset:4160
	ds_write_b32 v182, v25 offset:4416
	ds_write_b32 v182, v26 offset:4672
	ds_write_b32 v182, v27 offset:4928
	ds_write_b64 v173, v[34:35] offset:2336
	s_waitcnt lgkmcnt(15)
	v_mfma_f32_16x16x32_bf16 v[28:31], v[174:177], v[178:181], 0
	v_mfma_f32_16x16x32_bf16 v[28:31], v[240:243], v[244:247], v[28:31]
	s_nop 7
	ds_write_b32 v182, v28 offset:4224
	ds_write_b32 v182, v29 offset:4480
	ds_write_b32 v182, v30 offset:4736
	ds_write_b32 v182, v31 offset:4992
	v_cvt_pk_bf16_f32 v22, v28, v29
	v_cvt_pk_bf16_f32 v23, v30, v31
	ds_write_b64 v173, v[22:23] offset:4640
	s_waitcnt lgkmcnt(12)
	v_mfma_f32_16x16x32_bf16 v[24:27], v[2:5], v[6:9], 0
	s_waitcnt lgkmcnt(10)
	v_mfma_f32_16x16x32_bf16 v[24:27], v[10:13], v[14:17], v[24:27]
	s_nop 7
	ds_write_b32 v182, v24 offset:4288
	ds_write_b32 v182, v25 offset:4544
	ds_write_b32 v182, v26 offset:4800
	ds_write_b32 v182, v27 offset:5056
	v_cvt_pk_bf16_f32 v32, v24, v25
	v_cvt_pk_bf16_f32 v33, v26, v27
	ds_write_b64 v173, v[32:33] offset:6944
